# E1 and E2: each wave now pulls its own 8-token sub-item from the per-XCD queues (one atomic per wave, prefetched), no workgroup barriers or LDS slot inside the expert phases, so the two waves of a SIM
# speedup vs baseline: 1.0513x; 1.0198x over previous
.Le1w_first:
	s_mov_b64 exec, 1
	global_atomic_add v250, v211, v1, s[0:1] sc0
	s_mov_b64 exec, -1
	v_mov_b32_e32 v249, 0x80
	v_and_b32_e32 v235, 7, v0
	v_lshlrev_b32_e32 v218, 4, v235
	v_cmp_lt_u32_e64 s[38:39], 3, v235
	v_and_b32_e32 v238, 2, v0
	v_cmp_eq_u32_e64 s[40:41], 0, v238
	v_and_b32_e32 v238, 1, v0
	v_cmp_eq_u32_e64 s[42:43], 0, v238
	s_add_u32 s2, s96, 0x4c00000
	s_addc_u32 s3, s97, 0
	s_add_u32 s4, s96, 0x27600000
	s_addc_u32 s5, s97, 0
	s_add_u32 s4, s4, s80
	s_addc_u32 s5, s5, 0
	s_lshl_b32 s33, s60, 3
	s_waitcnt vmcnt(0)
	v_readfirstlane_b32 s35, v250
	s_cmp_ge_i32 s35, s33
	s_cbranch_scc1 .LBB0_722
	s_lshr_b32 s99, s35, 3
	s_lshl_b32 s98, s99, 6
	s_and_b32 s99, s99, 0xffffff00
	s_add_i32 s99, s99, 0x100
	s_and_b64 s[24:25], s[30:31], exec
	s_cselect_b32 s99, 0, s99
	s_add_i32 s98, s98, s99
	s_and_b32 s99, s35, 7
	s_lshl_b32 s99, s99, 3
	s_add_i32 s98, s98, s99
	v_and_b32_e32 v233, 63, v0
	v_and_b32_e32 v235, 7, v0
	v_bfe_u32 v236, v0, 3, 3
	s_lshl_b32 s99, s98, 8
	v_lshl_add_u32 v227, v233, 2, s99
	v_lshl_add_u32 v219, v236, 5, s99
	s_lshl_b32 s99, s98, 12
	s_add_i32 s99, s99, s76
	v_lshl_add_u32 v226, v235, 6, s99
	global_load_dwordx4 v[162:165], v219, s[22:23]
	global_load_dwordx4 v[166:169], v219, s[22:23] offset:16
	global_load_dwordx4 v[170:173], v219, s[22:23] offset:256
	global_load_dwordx4 v[174:177], v219, s[22:23] offset:272
	v_add_u32_e32 v219, 0x200, v219
	s_waitcnt vmcnt(2)
	v_mad_u32_u16 v194, v162, v249, v218
	v_mad_u32_u16 v195, v162, v249, v218 op_sel:[1,0,0,0]
	global_load_dwordx4 v[2:5], v194, s[10:11]
	global_load_dwordx4 v[6:9], v195, s[10:11]
	v_mad_u32_u16 v194, v163, v249, v218
	v_mad_u32_u16 v195, v163, v249, v218 op_sel:[1,0,0,0]
	global_load_dwordx4 v[10:13], v194, s[10:11]
	global_load_dwordx4 v[14:17], v195, s[10:11]
	v_mad_u32_u16 v194, v164, v249, v218
	v_mad_u32_u16 v195, v164, v249, v218 op_sel:[1,0,0,0]
	global_load_dwordx4 v[18:21], v194, s[10:11]
	global_load_dwordx4 v[22:25], v195, s[10:11]
	v_mad_u32_u16 v194, v165, v249, v218
	v_mad_u32_u16 v195, v165, v249, v218 op_sel:[1,0,0,0]
	global_load_dwordx4 v[26:29], v194, s[10:11]
	global_load_dwordx4 v[30:33], v195, s[10:11]
	v_mad_u32_u16 v194, v166, v249, v218
	v_mad_u32_u16 v195, v166, v249, v218 op_sel:[1,0,0,0]
	global_load_dwordx4 v[34:37], v194, s[10:11]
	global_load_dwordx4 v[38:41], v195, s[10:11]
	v_mad_u32_u16 v194, v167, v249, v218
	v_mad_u32_u16 v195, v167, v249, v218 op_sel:[1,0,0,0]
	global_load_dwordx4 v[42:45], v194, s[10:11]
	global_load_dwordx4 v[46:49], v195, s[10:11]
	v_mad_u32_u16 v194, v168, v249, v218
	v_mad_u32_u16 v195, v168, v249, v218 op_sel:[1,0,0,0]
	global_load_dwordx4 v[50:53], v194, s[10:11]
	global_load_dwordx4 v[54:57], v195, s[10:11]
	v_mad_u32_u16 v194, v169, v249, v218
	v_mad_u32_u16 v195, v169, v249, v218 op_sel:[1,0,0,0]
	global_load_dwordx4 v[58:61], v194, s[10:11]
	global_load_dwordx4 v[62:65], v195, s[10:11]
	global_load_dwordx4 v[130:133], v226, s[2:3]
	global_load_dwordx4 v[134:137], v226, s[2:3] offset:16
	global_load_dwordx4 v[138:141], v226, s[2:3] offset:32
	global_load_dwordx4 v[142:145], v226, s[2:3] offset:48
	s_mov_b32 s34, 0
	s_waitcnt vmcnt(0)
.Le1_loop:
	s_waitcnt vmcnt(1)
	v_mad_u32_u16 v194, v170, v249, v218
	v_mad_u32_u16 v195, v170, v249, v218 op_sel:[1,0,0,0]
	global_load_dwordx4 v[66:69], v194, s[10:11]
	global_load_dwordx4 v[70:73], v195, s[10:11]
	v_mad_u32_u16 v194, v171, v249, v218
	v_mad_u32_u16 v195, v171, v249, v218 op_sel:[1,0,0,0]
	global_load_dwordx4 v[74:77], v194, s[10:11]
	global_load_dwordx4 v[78:81], v195, s[10:11]
	v_mad_u32_u16 v194, v172, v249, v218
	v_mad_u32_u16 v195, v172, v249, v218 op_sel:[1,0,0,0]
	global_load_dwordx4 v[82:85], v194, s[10:11]
	global_load_dwordx4 v[86:89], v195, s[10:11]
	v_mad_u32_u16 v194, v173, v249, v218
	v_mad_u32_u16 v195, v173, v249, v218 op_sel:[1,0,0,0]
	global_load_dwordx4 v[90:93], v194, s[10:11]
	global_load_dwordx4 v[94:97], v195, s[10:11]
	v_mad_u32_u16 v194, v174, v249, v218
	v_mad_u32_u16 v195, v174, v249, v218 op_sel:[1,0,0,0]
	global_load_dwordx4 v[98:101], v194, s[10:11]
	global_load_dwordx4 v[102:105], v195, s[10:11]
	v_mad_u32_u16 v194, v175, v249, v218
	v_mad_u32_u16 v195, v175, v249, v218 op_sel:[1,0,0,0]
	global_load_dwordx4 v[106:109], v194, s[10:11]
	global_load_dwordx4 v[110:113], v195, s[10:11]
	v_mad_u32_u16 v194, v176, v249, v218
	v_mad_u32_u16 v195, v176, v249, v218 op_sel:[1,0,0,0]
	global_load_dwordx4 v[114:117], v194, s[10:11]
	global_load_dwordx4 v[118:121], v195, s[10:11]
	v_mad_u32_u16 v194, v177, v249, v218
	v_mad_u32_u16 v195, v177, v249, v218 op_sel:[1,0,0,0]
	global_load_dwordx4 v[122:125], v194, s[10:11]
	global_load_dwordx4 v[126:129], v195, s[10:11]
	v_add_u32_e32 v196, 0x1000, v226
	global_load_dwordx4 v[146:149], v196, s[2:3]
	global_load_dwordx4 v[150:153], v196, s[2:3] offset:16
	global_load_dwordx4 v[154:157], v196, s[2:3] offset:32
	global_load_dwordx4 v[158:161], v196, s[2:3] offset:48
	s_cmp_lt_u32 s34, 6
	s_cbranch_scc0 .Le1_A_last
	global_load_dwordx4 v[162:165], v219, s[22:23]
	global_load_dwordx4 v[166:169], v219, s[22:23] offset:16
	s_cmp_eq_u32 s34, 4
	s_cbranch_scc0 .Le1_A_done
	s_mov_b64 exec, 1
	global_atomic_add v250, v211, v1, s[0:1] sc0
	s_mov_b64 exec, -1
	s_branch .Le1_A_done
.Le1_A_last:
	v_readfirstlane_b32 s35, v250
	s_cmp_ge_i32 s35, s33
	s_cbranch_scc1 .Le1_A_nonext
	s_lshr_b32 s99, s35, 3
	s_lshl_b32 s98, s99, 6
	s_and_b32 s99, s99, 0xffffff00
	s_add_i32 s99, s99, 0x100
	s_and_b64 s[24:25], s[30:31], exec
	s_cselect_b32 s99, 0, s99
	s_add_i32 s98, s98, s99
	s_and_b32 s99, s35, 7
	s_lshl_b32 s99, s99, 3
	s_add_i32 s98, s98, s99
	v_and_b32_e32 v233, 63, v0
	v_and_b32_e32 v235, 7, v0
	v_bfe_u32 v236, v0, 3, 3
	s_lshl_b32 s99, s98, 8
	v_lshl_add_u32 v251, v233, 2, s99
	v_lshl_add_u32 v219, v236, 5, s99
	s_lshl_b32 s99, s98, 12
	s_add_i32 s99, s99, s76
	v_lshl_add_u32 v226, v235, 6, s99
	v_add_u32_e32 v226, 0xffffe000, v226
	global_load_dwordx4 v[162:165], v219, s[22:23]
	global_load_dwordx4 v[166:169], v219, s[22:23] offset:16
	global_load_dwordx4 v[170:173], v219, s[22:23] offset:256
	global_load_dwordx4 v[174:177], v219, s[22:23] offset:272
	v_add_u32_e32 v219, 0x200, v219
	s_branch .Le1_A_done

.Le1_B_issue:
	v_mad_u32_u16 v194, v162, v249, v218
	v_mad_u32_u16 v195, v162, v249, v218 op_sel:[1,0,0,0]
	global_load_dwordx4 v[2:5], v194, s[10:11]
	global_load_dwordx4 v[6:9], v195, s[10:11]
	v_mad_u32_u16 v194, v163, v249, v218
	v_mad_u32_u16 v195, v163, v249, v218 op_sel:[1,0,0,0]
	global_load_dwordx4 v[10:13], v194, s[10:11]
	global_load_dwordx4 v[14:17], v195, s[10:11]
	v_mad_u32_u16 v194, v164, v249, v218
	v_mad_u32_u16 v195, v164, v249, v218 op_sel:[1,0,0,0]
	global_load_dwordx4 v[18:21], v194, s[10:11]
	global_load_dwordx4 v[22:25], v195, s[10:11]
	v_mad_u32_u16 v194, v165, v249, v218
	v_mad_u32_u16 v195, v165, v249, v218 op_sel:[1,0,0,0]
	global_load_dwordx4 v[26:29], v194, s[10:11]
	global_load_dwordx4 v[30:33], v195, s[10:11]
	v_mad_u32_u16 v194, v166, v249, v218
	v_mad_u32_u16 v195, v166, v249, v218 op_sel:[1,0,0,0]
	global_load_dwordx4 v[34:37], v194, s[10:11]
	global_load_dwordx4 v[38:41], v195, s[10:11]
	v_mad_u32_u16 v194, v167, v249, v218
	v_mad_u32_u16 v195, v167, v249, v218 op_sel:[1,0,0,0]
	global_load_dwordx4 v[42:45], v194, s[10:11]
	global_load_dwordx4 v[46:49], v195, s[10:11]
	v_mad_u32_u16 v194, v168, v249, v218
	v_mad_u32_u16 v195, v168, v249, v218 op_sel:[1,0,0,0]
	global_load_dwordx4 v[50:53], v194, s[10:11]
	global_load_dwordx4 v[54:57], v195, s[10:11]
	v_mad_u32_u16 v194, v169, v249, v218
	v_mad_u32_u16 v195, v169, v249, v218 op_sel:[1,0,0,0]
	global_load_dwordx4 v[58:61], v194, s[10:11]
	global_load_dwordx4 v[62:65], v195, s[10:11]
	v_add_u32_e32 v196, 0x2000, v226
	global_load_dwordx4 v[130:133], v196, s[2:3]
	global_load_dwordx4 v[134:137], v196, s[2:3] offset:16
	global_load_dwordx4 v[138:141], v196, s[2:3] offset:32
	global_load_dwordx4 v[142:145], v196, s[2:3] offset:48
	s_cmp_lt_u32 s34, 6
	s_cbranch_scc0 .Le1_B_done
	global_load_dwordx4 v[170:173], v219, s[22:23] offset:256
	global_load_dwordx4 v[174:177], v219, s[22:23] offset:272
	v_add_u32_e32 v219, 0x200, v219

.Le2w_first:
	s_mov_b64 exec, 1
	global_atomic_add v251, v211, v1, s[24:25] sc0
	s_mov_b64 exec, -1
	s_movk_i32 s34, 0x80
	v_and_b32_e32 v242, 7, v0
	v_bfe_u32 v245, v0, 3, 1
	v_lshlrev_b32_e32 v218, 4, v242
	v_lshl_or_b32 v246, v242, 5, s58
	v_lshrrev_b32_e32 v247, 1, v0
	v_and_b32_e32 v247, 24, v247
	v_lshlrev_b32_e32 v248, 2, v245
	v_or3_b32 v246, v246, v247, v248
	v_lshlrev_b32_e32 v236, 2, v246
	v_mov_b32_e32 v237, 0
	v_cmp_eq_u32_e64 s[38:39], 0, v245
	s_lshl_b32 s42, s60, 3
	s_waitcnt vmcnt(0)
	v_readfirstlane_b32 s35, v251
	s_cmp_ge_i32 s35, s42
	s_cbranch_scc1 .LBB0_878
	s_lshr_b32 s99, s35, 3
	s_lshl_b32 s98, s99, 6
	s_and_b32 s99, s99, 0xffffff00
	s_add_i32 s99, s99, 0x100
	s_and_b64 s[0:1], s[30:31], exec
	s_cselect_b32 s99, 0, s99
	s_add_i32 s98, s98, s99
	s_and_b32 s99, s35, 7
	s_lshl_b32 s99, s99, 3
	s_add_i32 s98, s98, s99
	v_bfe_u32 v244, v0, 3, 3
	v_mov_b32_e32 v226, s98
	s_lshl_b32 s99, s98, 8
	v_lshl_add_u32 v219, v244, 5, s99
	global_load_dwordx4 v[162:165], v219, s[22:23]
	global_load_dwordx4 v[166:169], v219, s[22:23] offset:16
	global_load_dwordx4 v[170:173], v219, s[22:23] offset:256
	global_load_dwordx4 v[174:177], v219, s[22:23] offset:272
	s_waitcnt vmcnt(2)
	v_mad_u32_u16 v194, v162, s34, v218
	v_mad_u32_u16 v195, v162, s34, v218 op_sel:[1,0,0,0]
	global_load_dwordx4 v[2:5], v194, s[40:41]
	global_load_dwordx4 v[6:9], v195, s[40:41]
	v_mad_u32_u16 v194, v163, s34, v218
	v_mad_u32_u16 v195, v163, s34, v218 op_sel:[1,0,0,0]
	global_load_dwordx4 v[10:13], v194, s[40:41]
	global_load_dwordx4 v[14:17], v195, s[40:41]
	v_mad_u32_u16 v194, v164, s34, v218
	v_mad_u32_u16 v195, v164, s34, v218 op_sel:[1,0,0,0]
	global_load_dwordx4 v[18:21], v194, s[40:41]
	global_load_dwordx4 v[22:25], v195, s[40:41]
	v_mad_u32_u16 v194, v165, s34, v218
	v_mad_u32_u16 v195, v165, s34, v218 op_sel:[1,0,0,0]
	global_load_dwordx4 v[26:29], v194, s[40:41]
	global_load_dwordx4 v[30:33], v195, s[40:41]
	v_mad_u32_u16 v194, v166, s34, v218
	v_mad_u32_u16 v195, v166, s34, v218 op_sel:[1,0,0,0]
	global_load_dwordx4 v[34:37], v194, s[40:41]
	global_load_dwordx4 v[38:41], v195, s[40:41]
	v_mad_u32_u16 v194, v167, s34, v218
	v_mad_u32_u16 v195, v167, s34, v218 op_sel:[1,0,0,0]
	global_load_dwordx4 v[42:45], v194, s[40:41]
	global_load_dwordx4 v[46:49], v195, s[40:41]
	v_mad_u32_u16 v194, v168, s34, v218
	v_mad_u32_u16 v195, v168, s34, v218 op_sel:[1,0,0,0]
	global_load_dwordx4 v[50:53], v194, s[40:41]
	global_load_dwordx4 v[54:57], v195, s[40:41]
	v_mad_u32_u16 v194, v169, s34, v218
	v_mad_u32_u16 v195, v169, s34, v218 op_sel:[1,0,0,0]
	global_load_dwordx4 v[58:61], v194, s[40:41]
	global_load_dwordx4 v[62:65], v195, s[40:41]
	global_load_dwordx4 v[130:133], v219, s[56:57] offset:-272
	global_load_dwordx4 v[134:137], v219, s[56:57] offset:-256
	v_add_u32_e32 v250, 0, v226
	v_mul_hi_i32 v242, v250, s69
	v_lshrrev_b32_e32 v243, 31, v242
	v_ashrrev_i32_e32 v242, 13, v242
	v_add_u32_e32 v243, v242, v243
	v_mul_i32_i24_e32 v246, 0xffffbf00, v243
	v_add_u32_e32 v242, v250, v246
	v_cmp_gt_i32_e32 vcc, s68, v242
	v_cmp_lt_i32_e64 s[0:1], s21, v242
	s_and_saveexec_b64 s[2:3], s[0:1]
	s_xor_b64 s[0:1], exec, s[2:3]
	v_lshl_add_u32 v242, v243, 14, v246
	v_add3_u32 v242, v250, v242, s88
	s_or_saveexec_b64 s[0:1], s[0:1]
	v_mov_b64_e32 v[244:245], s[18:19]
	s_xor_b64 exec, exec, s[0:1]
	v_lshlrev_b32_e32 v242, 8, v243
	v_add3_u32 v242, v246, v250, v242
	v_mov_b64_e32 v[244:245], s[72:73]
	s_or_b64 exec, exec, s[0:1]
	v_mul_i32_i24_e32 v243, 0x3000, v243
	v_cndmask_b32_e32 v246, v243, v223, vcc
	v_ashrrev_i32_e32 v247, 31, v246
	v_lshl_add_u64 v[246:247], v[246:247], 2, s[10:11]
	v_ashrrev_i32_e32 v243, 31, v242
	v_lshl_add_u64 v[248:249], v[246:247], 0, v[236:237]
	v_lshlrev_b64 v[242:243], 13, v[242:243]
	v_lshl_add_u64 v[242:243], v[244:245], 0, v[242:243]
	v_add_co_u32_e32 v248, vcc, s94, v248
	v_lshl_add_u64 v[238:239], v[242:243], 0, v[236:237]
	s_nop 0
	v_addc_co_u32_e32 v249, vcc, 0, v249, vcc
	global_load_dwordx4 v[146:149], v[238:239], off
	global_load_dwordx4 v[150:153], v[248:249], off
	v_add_u32_e32 v219, 0x200, v219
	s_mov_b32 s33, 0
	s_waitcnt vmcnt(0)
.Le2_loop:
	s_waitcnt vmcnt(1)
	v_mad_u32_u16 v194, v170, s34, v218
	v_mad_u32_u16 v195, v170, s34, v218 op_sel:[1,0,0,0]
	global_load_dwordx4 v[66:69], v194, s[40:41]
	global_load_dwordx4 v[70:73], v195, s[40:41]
	v_mad_u32_u16 v194, v171, s34, v218
	v_mad_u32_u16 v195, v171, s34, v218 op_sel:[1,0,0,0]
	global_load_dwordx4 v[74:77], v194, s[40:41]
	global_load_dwordx4 v[78:81], v195, s[40:41]
	v_mad_u32_u16 v194, v172, s34, v218
	v_mad_u32_u16 v195, v172, s34, v218 op_sel:[1,0,0,0]
	global_load_dwordx4 v[82:85], v194, s[40:41]
	global_load_dwordx4 v[86:89], v195, s[40:41]
	v_mad_u32_u16 v194, v173, s34, v218
	v_mad_u32_u16 v195, v173, s34, v218 op_sel:[1,0,0,0]
	global_load_dwordx4 v[90:93], v194, s[40:41]
	global_load_dwordx4 v[94:97], v195, s[40:41]
	v_mad_u32_u16 v194, v174, s34, v218
	v_mad_u32_u16 v195, v174, s34, v218 op_sel:[1,0,0,0]
	global_load_dwordx4 v[98:101], v194, s[40:41]
	global_load_dwordx4 v[102:105], v195, s[40:41]
	v_mad_u32_u16 v194, v175, s34, v218
	v_mad_u32_u16 v195, v175, s34, v218 op_sel:[1,0,0,0]
	global_load_dwordx4 v[106:109], v194, s[40:41]
	global_load_dwordx4 v[110:113], v195, s[40:41]
	v_mad_u32_u16 v194, v176, s34, v218
	v_mad_u32_u16 v195, v176, s34, v218 op_sel:[1,0,0,0]
	global_load_dwordx4 v[114:117], v194, s[40:41]
	global_load_dwordx4 v[118:121], v195, s[40:41]
	v_mad_u32_u16 v194, v177, s34, v218
	v_mad_u32_u16 v195, v177, s34, v218 op_sel:[1,0,0,0]
	global_load_dwordx4 v[122:125], v194, s[40:41]
	global_load_dwordx4 v[126:129], v195, s[40:41]
	global_load_dwordx4 v[138:141], v219, s[56:57] offset:-528
	global_load_dwordx4 v[142:145], v219, s[56:57] offset:-512
	v_lshl_add_u64 v[240:241], v[238:239], 0, s[48:49]
	global_load_dwordx4 v[158:161], v[248:249], off
	global_load_dwordx4 v[154:157], v[240:241], off
	s_cmp_lt_u32 s33, 6
	s_cbranch_scc0 .Le2_A_last
	global_load_dwordx4 v[162:165], v219, s[22:23]
	global_load_dwordx4 v[166:169], v219, s[22:23] offset:16
	s_cmp_eq_u32 s33, 4
	s_cbranch_scc0 .Le2_A_done
	s_mov_b64 exec, 1
	global_atomic_add v251, v211, v1, s[24:25] sc0
	s_mov_b64 exec, -1
	s_branch .Le2_A_done
.Le2_A_last:
	v_readfirstlane_b32 s35, v251
	s_cmp_ge_i32 s35, s42
	s_cbranch_scc1 .Le2_A_nonext
	s_lshr_b32 s99, s35, 3
	s_lshl_b32 s98, s99, 6
	s_and_b32 s99, s99, 0xffffff00
	s_add_i32 s99, s99, 0x100
	s_and_b64 s[0:1], s[30:31], exec
	s_cselect_b32 s99, 0, s99
	s_add_i32 s98, s98, s99
	s_and_b32 s99, s35, 7
	s_lshl_b32 s99, s99, 3
	s_add_i32 s98, s98, s99
	v_bfe_u32 v244, v0, 3, 3
	s_lshl_b32 s99, s98, 8
	v_lshl_add_u32 v219, v244, 5, s99
	s_add_i32 s99, s98, -2
	v_mov_b32_e32 v226, s99
	global_load_dwordx4 v[162:165], v219, s[22:23]
	global_load_dwordx4 v[166:169], v219, s[22:23] offset:16
	global_load_dwordx4 v[170:173], v219, s[22:23] offset:256
	global_load_dwordx4 v[174:177], v219, s[22:23] offset:272
	s_branch .Le2_A_done

.Le2_B_issue:
	v_mad_u32_u16 v194, v162, s34, v218
	v_mad_u32_u16 v195, v162, s34, v218 op_sel:[1,0,0,0]
	global_load_dwordx4 v[2:5], v194, s[40:41]
	global_load_dwordx4 v[6:9], v195, s[40:41]
	v_mad_u32_u16 v194, v163, s34, v218
	v_mad_u32_u16 v195, v163, s34, v218 op_sel:[1,0,0,0]
	global_load_dwordx4 v[10:13], v194, s[40:41]
	global_load_dwordx4 v[14:17], v195, s[40:41]
	v_mad_u32_u16 v194, v164, s34, v218
	v_mad_u32_u16 v195, v164, s34, v218 op_sel:[1,0,0,0]
	global_load_dwordx4 v[18:21], v194, s[40:41]
	global_load_dwordx4 v[22:25], v195, s[40:41]
	v_mad_u32_u16 v194, v165, s34, v218
	v_mad_u32_u16 v195, v165, s34, v218 op_sel:[1,0,0,0]
	global_load_dwordx4 v[26:29], v194, s[40:41]
	global_load_dwordx4 v[30:33], v195, s[40:41]
	v_mad_u32_u16 v194, v166, s34, v218
	v_mad_u32_u16 v195, v166, s34, v218 op_sel:[1,0,0,0]
	global_load_dwordx4 v[34:37], v194, s[40:41]
	global_load_dwordx4 v[38:41], v195, s[40:41]
	v_mad_u32_u16 v194, v167, s34, v218
	v_mad_u32_u16 v195, v167, s34, v218 op_sel:[1,0,0,0]
	global_load_dwordx4 v[42:45], v194, s[40:41]
	global_load_dwordx4 v[46:49], v195, s[40:41]
	v_mad_u32_u16 v194, v168, s34, v218
	v_mad_u32_u16 v195, v168, s34, v218 op_sel:[1,0,0,0]
	global_load_dwordx4 v[50:53], v194, s[40:41]
	global_load_dwordx4 v[54:57], v195, s[40:41]
	v_mad_u32_u16 v194, v169, s34, v218
	v_mad_u32_u16 v195, v169, s34, v218 op_sel:[1,0,0,0]
	global_load_dwordx4 v[58:61], v194, s[40:41]
	global_load_dwordx4 v[62:65], v195, s[40:41]
	global_load_dwordx4 v[130:133], v219, s[56:57] offset:-272
	global_load_dwordx4 v[134:137], v219, s[56:57] offset:-256
	s_cmp_lt_u32 s33, 6
	s_cbranch_scc0 .Le2_B_chainx
	v_lshl_add_u64 v[238:239], v[240:241], 0, s[48:49]
	global_load_dwordx4 v[150:153], v[248:249], off
	global_load_dwordx4 v[146:149], v[238:239], off
	global_load_dwordx4 v[170:173], v219, s[22:23] offset:256
	global_load_dwordx4 v[174:177], v219, s[22:23] offset:272
	s_branch .Le2_B_noids
.Le2_B_chainx:
	v_add_u32_e32 v250, 2, v226
	v_mul_hi_i32 v242, v250, s69
	v_lshrrev_b32_e32 v243, 31, v242
	v_ashrrev_i32_e32 v242, 13, v242
	v_add_u32_e32 v243, v242, v243
	v_mul_i32_i24_e32 v246, 0xffffbf00, v243
	v_add_u32_e32 v242, v250, v246
	v_cmp_gt_i32_e32 vcc, s68, v242
	v_cmp_lt_i32_e64 s[0:1], s21, v242
	s_and_saveexec_b64 s[2:3], s[0:1]
	s_xor_b64 s[0:1], exec, s[2:3]
	v_lshl_add_u32 v242, v243, 14, v246
	v_add3_u32 v242, v250, v242, s88
	s_or_saveexec_b64 s[0:1], s[0:1]
	v_mov_b64_e32 v[244:245], s[18:19]
	s_xor_b64 exec, exec, s[0:1]
	v_lshlrev_b32_e32 v242, 8, v243
	v_add3_u32 v242, v246, v250, v242
	v_mov_b64_e32 v[244:245], s[72:73]
	s_or_b64 exec, exec, s[0:1]
	v_mul_i32_i24_e32 v243, 0x3000, v243
	v_cndmask_b32_e32 v246, v243, v223, vcc
	v_ashrrev_i32_e32 v247, 31, v246
	v_lshl_add_u64 v[246:247], v[246:247], 2, s[10:11]
	v_ashrrev_i32_e32 v243, 31, v242
	v_lshl_add_u64 v[248:249], v[246:247], 0, v[236:237]
	v_lshlrev_b64 v[242:243], 13, v[242:243]
	v_lshl_add_u64 v[242:243], v[244:245], 0, v[242:243]
	v_add_co_u32_e32 v248, vcc, s94, v248
	v_lshl_add_u64 v[238:239], v[242:243], 0, v[236:237]
	s_nop 0
	v_addc_co_u32_e32 v249, vcc, 0, v249, vcc
	global_load_dwordx4 v[146:149], v[238:239], off
	global_load_dwordx4 v[150:153], v[248:249], off
.Le2_B_noids:
	v_add_u32_e32 v219, 0x200, v219
.Le2_B_done:
	v_mul_u32_u24_sdwa v202, v138, s93 dst_sel:DWORD dst_unused:UNUSED_PAD src0_sel:WORD_0 src1_sel:DWORD
	v_cvt_scalef32_pk_f16_fp4 v194, v66, 1.0
	v_cvt_scalef32_pk_f16_fp4 v195, v66, 1.0 op_sel:[1,0,0]
	v_cvt_scalef32_pk_f16_fp4 v196, v66, 1.0 op_sel:[0,1,0]
	v_pk_fma_f16 v178, v194, v202, 0
	v_cvt_scalef32_pk_f16_fp4 v197, v66, 1.0 op_sel:[1,1,0]
	v_pk_fma_f16 v179, v195, v202, 0
	v_cvt_scalef32_pk_f16_fp4 v194, v67, 1.0
	v_pk_fma_f16 v180, v196, v202, 0
	v_cvt_scalef32_pk_f16_fp4 v195, v67, 1.0 op_sel:[1,0,0]
	v_pk_fma_f16 v181, v197, v202, 0
	v_cvt_scalef32_pk_f16_fp4 v196, v67, 1.0 op_sel:[0,1,0]
	v_pk_fma_f16 v182, v194, v202, 0
	v_cvt_scalef32_pk_f16_fp4 v197, v67, 1.0 op_sel:[1,1,0]
	v_pk_fma_f16 v183, v195, v202, 0
	v_cvt_scalef32_pk_f16_fp4 v194, v68, 1.0
	v_pk_fma_f16 v184, v196, v202, 0
	v_cvt_scalef32_pk_f16_fp4 v195, v68, 1.0 op_sel:[1,0,0]
	v_pk_fma_f16 v185, v197, v202, 0
	v_cvt_scalef32_pk_f16_fp4 v196, v68, 1.0 op_sel:[0,1,0]
	v_pk_fma_f16 v186, v194, v202, 0
	v_cvt_scalef32_pk_f16_fp4 v197, v68, 1.0 op_sel:[1,1,0]
	v_pk_fma_f16 v187, v195, v202, 0
	v_cvt_scalef32_pk_f16_fp4 v194, v69, 1.0
	v_pk_fma_f16 v188, v196, v202, 0
	v_cvt_scalef32_pk_f16_fp4 v195, v69, 1.0 op_sel:[1,0,0]
	v_pk_fma_f16 v189, v197, v202, 0
	v_cvt_scalef32_pk_f16_fp4 v196, v69, 1.0 op_sel:[0,1,0]
	v_pk_fma_f16 v190, v194, v202, 0
	v_cvt_scalef32_pk_f16_fp4 v197, v69, 1.0 op_sel:[1,1,0]
	v_pk_fma_f16 v191, v195, v202, 0
	v_pk_fma_f16 v192, v196, v202, 0
	v_pk_fma_f16 v193, v197, v202, 0
	v_mul_u32_u24_sdwa v203, v138, s93 dst_sel:DWORD dst_unused:UNUSED_PAD src0_sel:WORD_1 src1_sel:DWORD
	v_cvt_scalef32_pk_f16_fp4 v194, v70, 1.0
	v_cvt_scalef32_pk_f16_fp4 v195, v70, 1.0 op_sel:[1,0,0]
	v_cvt_scalef32_pk_f16_fp4 v196, v70, 1.0 op_sel:[0,1,0]
	v_pk_fma_f16 v178, v194, v203, v178
	v_cvt_scalef32_pk_f16_fp4 v197, v70, 1.0 op_sel:[1,1,0]
	v_pk_fma_f16 v179, v195, v203, v179
	v_cvt_scalef32_pk_f16_fp4 v194, v71, 1.0
	v_pk_fma_f16 v180, v196, v203, v180
	v_cvt_scalef32_pk_f16_fp4 v195, v71, 1.0 op_sel:[1,0,0]
	v_pk_fma_f16 v181, v197, v203, v181
	v_cvt_scalef32_pk_f16_fp4 v196, v71, 1.0 op_sel:[0,1,0]
	v_pk_fma_f16 v182, v194, v203, v182
	v_cvt_scalef32_pk_f16_fp4 v197, v71, 1.0 op_sel:[1,1,0]
	v_pk_fma_f16 v183, v195, v203, v183
	v_cvt_scalef32_pk_f16_fp4 v194, v72, 1.0
	v_pk_fma_f16 v184, v196, v203, v184
	v_cvt_scalef32_pk_f16_fp4 v195, v72, 1.0 op_sel:[1,0,0]
	v_pk_fma_f16 v185, v197, v203, v185
	v_cvt_scalef32_pk_f16_fp4 v196, v72, 1.0 op_sel:[0,1,0]
	v_pk_fma_f16 v186, v194, v203, v186
	v_cvt_scalef32_pk_f16_fp4 v197, v72, 1.0 op_sel:[1,1,0]
	v_pk_fma_f16 v187, v195, v203, v187
	v_cvt_scalef32_pk_f16_fp4 v194, v73, 1.0
	v_pk_fma_f16 v188, v196, v203, v188
	v_cvt_scalef32_pk_f16_fp4 v195, v73, 1.0 op_sel:[1,0,0]
	v_pk_fma_f16 v189, v197, v203, v189
	v_cvt_scalef32_pk_f16_fp4 v196, v73, 1.0 op_sel:[0,1,0]
	v_pk_fma_f16 v190, v194, v203, v190
	v_cvt_scalef32_pk_f16_fp4 v197, v73, 1.0 op_sel:[1,1,0]
	v_pk_fma_f16 v191, v195, v203, v191
	v_pk_fma_f16 v192, v196, v203, v192
	v_pk_fma_f16 v193, v197, v203, v193
	v_mul_u32_u24_sdwa v202, v139, s93 dst_sel:DWORD dst_unused:UNUSED_PAD src0_sel:WORD_0 src1_sel:DWORD
	v_cvt_scalef32_pk_f16_fp4 v194, v74, 1.0
	v_cvt_scalef32_pk_f16_fp4 v195, v74, 1.0 op_sel:[1,0,0]
	v_cvt_scalef32_pk_f16_fp4 v196, v74, 1.0 op_sel:[0,1,0]
	v_pk_fma_f16 v178, v194, v202, v178
	v_cvt_scalef32_pk_f16_fp4 v197, v74, 1.0 op_sel:[1,1,0]
	v_pk_fma_f16 v179, v195, v202, v179
	v_cvt_scalef32_pk_f16_fp4 v194, v75, 1.0
	v_pk_fma_f16 v180, v196, v202, v180
	v_cvt_scalef32_pk_f16_fp4 v195, v75, 1.0 op_sel:[1,0,0]
	v_pk_fma_f16 v181, v197, v202, v181
	v_cvt_scalef32_pk_f16_fp4 v196, v75, 1.0 op_sel:[0,1,0]
	v_pk_fma_f16 v182, v194, v202, v182
	v_cvt_scalef32_pk_f16_fp4 v197, v75, 1.0 op_sel:[1,1,0]
	v_pk_fma_f16 v183, v195, v202, v183
	v_cvt_scalef32_pk_f16_fp4 v194, v76, 1.0
	v_pk_fma_f16 v184, v196, v202, v184
	v_cvt_scalef32_pk_f16_fp4 v195, v76, 1.0 op_sel:[1,0,0]
	v_pk_fma_f16 v185, v197, v202, v185
	v_cvt_scalef32_pk_f16_fp4 v196, v76, 1.0 op_sel:[0,1,0]
	v_pk_fma_f16 v186, v194, v202, v186
	v_cvt_scalef32_pk_f16_fp4 v197, v76, 1.0 op_sel:[1,1,0]
	v_pk_fma_f16 v187, v195, v202, v187
	v_cvt_scalef32_pk_f16_fp4 v194, v77, 1.0
	v_pk_fma_f16 v188, v196, v202, v188
	v_cvt_scalef32_pk_f16_fp4 v195, v77, 1.0 op_sel:[1,0,0]
	v_pk_fma_f16 v189, v197, v202, v189
	v_cvt_scalef32_pk_f16_fp4 v196, v77, 1.0 op_sel:[0,1,0]
	v_pk_fma_f16 v190, v194, v202, v190
	v_cvt_scalef32_pk_f16_fp4 v197, v77, 1.0 op_sel:[1,1,0]
	v_pk_fma_f16 v191, v195, v202, v191
	v_pk_fma_f16 v192, v196, v202, v192
	v_pk_fma_f16 v193, v197, v202, v193
	v_mul_u32_u24_sdwa v203, v139, s93 dst_sel:DWORD dst_unused:UNUSED_PAD src0_sel:WORD_1 src1_sel:DWORD
	v_cvt_scalef32_pk_f16_fp4 v194, v78, 1.0
	v_cvt_scalef32_pk_f16_fp4 v195, v78, 1.0 op_sel:[1,0,0]
	v_cvt_scalef32_pk_f16_fp4 v196, v78, 1.0 op_sel:[0,1,0]
	v_pk_fma_f16 v178, v194, v203, v178
	v_cvt_scalef32_pk_f16_fp4 v197, v78, 1.0 op_sel:[1,1,0]
	v_pk_fma_f16 v179, v195, v203, v179
	v_cvt_scalef32_pk_f16_fp4 v194, v79, 1.0
	v_pk_fma_f16 v180, v196, v203, v180
	v_cvt_scalef32_pk_f16_fp4 v195, v79, 1.0 op_sel:[1,0,0]
	v_pk_fma_f16 v181, v197, v203, v181
	v_cvt_scalef32_pk_f16_fp4 v196, v79, 1.0 op_sel:[0,1,0]
	v_pk_fma_f16 v182, v194, v203, v182
	v_cvt_scalef32_pk_f16_fp4 v197, v79, 1.0 op_sel:[1,1,0]
	v_pk_fma_f16 v183, v195, v203, v183
	v_cvt_scalef32_pk_f16_fp4 v194, v80, 1.0
	v_pk_fma_f16 v184, v196, v203, v184
	v_cvt_scalef32_pk_f16_fp4 v195, v80, 1.0 op_sel:[1,0,0]
	v_pk_fma_f16 v185, v197, v203, v185
	v_cvt_scalef32_pk_f16_fp4 v196, v80, 1.0 op_sel:[0,1,0]
	v_pk_fma_f16 v186, v194, v203, v186
	v_cvt_scalef32_pk_f16_fp4 v197, v80, 1.0 op_sel:[1,1,0]
	v_pk_fma_f16 v187, v195, v203, v187
	v_cvt_scalef32_pk_f16_fp4 v194, v81, 1.0
	v_pk_fma_f16 v188, v196, v203, v188
	v_cvt_scalef32_pk_f16_fp4 v195, v81, 1.0 op_sel:[1,0,0]
	v_pk_fma_f16 v189, v197, v203, v189
	v_cvt_scalef32_pk_f16_fp4 v196, v81, 1.0 op_sel:[0,1,0]
	v_pk_fma_f16 v190, v194, v203, v190
	v_cvt_scalef32_pk_f16_fp4 v197, v81, 1.0 op_sel:[1,1,0]
	v_pk_fma_f16 v191, v195, v203, v191
	v_pk_fma_f16 v192, v196, v203, v192
	v_pk_fma_f16 v193, v197, v203, v193
	v_mul_u32_u24_sdwa v202, v140, s93 dst_sel:DWORD dst_unused:UNUSED_PAD src0_sel:WORD_0 src1_sel:DWORD
	v_cvt_scalef32_pk_f16_fp4 v194, v82, 1.0
	v_cvt_scalef32_pk_f16_fp4 v195, v82, 1.0 op_sel:[1,0,0]
	v_cvt_scalef32_pk_f16_fp4 v196, v82, 1.0 op_sel:[0,1,0]
	v_pk_fma_f16 v178, v194, v202, v178
	v_cvt_scalef32_pk_f16_fp4 v197, v82, 1.0 op_sel:[1,1,0]
	v_pk_fma_f16 v179, v195, v202, v179
	v_cvt_scalef32_pk_f16_fp4 v194, v83, 1.0
	v_pk_fma_f16 v180, v196, v202, v180
	v_cvt_scalef32_pk_f16_fp4 v195, v83, 1.0 op_sel:[1,0,0]
	v_pk_fma_f16 v181, v197, v202, v181
	v_cvt_scalef32_pk_f16_fp4 v196, v83, 1.0 op_sel:[0,1,0]
	v_pk_fma_f16 v182, v194, v202, v182
	v_cvt_scalef32_pk_f16_fp4 v197, v83, 1.0 op_sel:[1,1,0]
	v_pk_fma_f16 v183, v195, v202, v183
	v_cvt_scalef32_pk_f16_fp4 v194, v84, 1.0
	v_pk_fma_f16 v184, v196, v202, v184
	v_cvt_scalef32_pk_f16_fp4 v195, v84, 1.0 op_sel:[1,0,0]
	v_pk_fma_f16 v185, v197, v202, v185
	v_cvt_scalef32_pk_f16_fp4 v196, v84, 1.0 op_sel:[0,1,0]
	v_pk_fma_f16 v186, v194, v202, v186
	v_cvt_scalef32_pk_f16_fp4 v197, v84, 1.0 op_sel:[1,1,0]
	v_pk_fma_f16 v187, v195, v202, v187
	v_cvt_scalef32_pk_f16_fp4 v194, v85, 1.0
	v_pk_fma_f16 v188, v196, v202, v188
	v_cvt_scalef32_pk_f16_fp4 v195, v85, 1.0 op_sel:[1,0,0]
	v_pk_fma_f16 v189, v197, v202, v189
	v_cvt_scalef32_pk_f16_fp4 v196, v85, 1.0 op_sel:[0,1,0]
	v_pk_fma_f16 v190, v194, v202, v190
	v_cvt_scalef32_pk_f16_fp4 v197, v85, 1.0 op_sel:[1,1,0]
	v_pk_fma_f16 v191, v195, v202, v191
	v_pk_fma_f16 v192, v196, v202, v192
	v_pk_fma_f16 v193, v197, v202, v193
	v_mul_u32_u24_sdwa v203, v140, s93 dst_sel:DWORD dst_unused:UNUSED_PAD src0_sel:WORD_1 src1_sel:DWORD
	v_cvt_scalef32_pk_f16_fp4 v194, v86, 1.0
	v_cvt_scalef32_pk_f16_fp4 v195, v86, 1.0 op_sel:[1,0,0]
	v_cvt_scalef32_pk_f16_fp4 v196, v86, 1.0 op_sel:[0,1,0]
	v_pk_fma_f16 v178, v194, v203, v178
	v_cvt_scalef32_pk_f16_fp4 v197, v86, 1.0 op_sel:[1,1,0]
	v_pk_fma_f16 v179, v195, v203, v179
	v_cvt_scalef32_pk_f16_fp4 v194, v87, 1.0
	v_pk_fma_f16 v180, v196, v203, v180
	v_cvt_scalef32_pk_f16_fp4 v195, v87, 1.0 op_sel:[1,0,0]
	v_pk_fma_f16 v181, v197, v203, v181
	v_cvt_scalef32_pk_f16_fp4 v196, v87, 1.0 op_sel:[0,1,0]
	v_pk_fma_f16 v182, v194, v203, v182
	v_cvt_scalef32_pk_f16_fp4 v197, v87, 1.0 op_sel:[1,1,0]
	v_pk_fma_f16 v183, v195, v203, v183
	v_cvt_scalef32_pk_f16_fp4 v194, v88, 1.0
	v_pk_fma_f16 v184, v196, v203, v184
	v_cvt_scalef32_pk_f16_fp4 v195, v88, 1.0 op_sel:[1,0,0]
	v_pk_fma_f16 v185, v197, v203, v185
	v_cvt_scalef32_pk_f16_fp4 v196, v88, 1.0 op_sel:[0,1,0]
	v_pk_fma_f16 v186, v194, v203, v186
	v_cvt_scalef32_pk_f16_fp4 v197, v88, 1.0 op_sel:[1,1,0]
	v_pk_fma_f16 v187, v195, v203, v187
	v_cvt_scalef32_pk_f16_fp4 v194, v89, 1.0
	v_pk_fma_f16 v188, v196, v203, v188
	v_cvt_scalef32_pk_f16_fp4 v195, v89, 1.0 op_sel:[1,0,0]
	v_pk_fma_f16 v189, v197, v203, v189
	v_cvt_scalef32_pk_f16_fp4 v196, v89, 1.0 op_sel:[0,1,0]
	v_pk_fma_f16 v190, v194, v203, v190
	v_cvt_scalef32_pk_f16_fp4 v197, v89, 1.0 op_sel:[1,1,0]
	v_pk_fma_f16 v191, v195, v203, v191
	v_pk_fma_f16 v192, v196, v203, v192
	v_pk_fma_f16 v193, v197, v203, v193
	v_mul_u32_u24_sdwa v202, v141, s93 dst_sel:DWORD dst_unused:UNUSED_PAD src0_sel:WORD_0 src1_sel:DWORD
	v_cvt_scalef32_pk_f16_fp4 v194, v90, 1.0
	v_cvt_scalef32_pk_f16_fp4 v195, v90, 1.0 op_sel:[1,0,0]
	v_cvt_scalef32_pk_f16_fp4 v196, v90, 1.0 op_sel:[0,1,0]
	v_pk_fma_f16 v178, v194, v202, v178
	v_cvt_scalef32_pk_f16_fp4 v197, v90, 1.0 op_sel:[1,1,0]
	v_pk_fma_f16 v179, v195, v202, v179
	v_cvt_scalef32_pk_f16_fp4 v194, v91, 1.0
	v_pk_fma_f16 v180, v196, v202, v180
	v_cvt_scalef32_pk_f16_fp4 v195, v91, 1.0 op_sel:[1,0,0]
	v_pk_fma_f16 v181, v197, v202, v181
	v_cvt_scalef32_pk_f16_fp4 v196, v91, 1.0 op_sel:[0,1,0]
	v_pk_fma_f16 v182, v194, v202, v182
	v_cvt_scalef32_pk_f16_fp4 v197, v91, 1.0 op_sel:[1,1,0]
	v_pk_fma_f16 v183, v195, v202, v183
	v_cvt_scalef32_pk_f16_fp4 v194, v92, 1.0
	v_pk_fma_f16 v184, v196, v202, v184
	v_cvt_scalef32_pk_f16_fp4 v195, v92, 1.0 op_sel:[1,0,0]
	v_pk_fma_f16 v185, v197, v202, v185
	v_cvt_scalef32_pk_f16_fp4 v196, v92, 1.0 op_sel:[0,1,0]
	v_pk_fma_f16 v186, v194, v202, v186
	v_cvt_scalef32_pk_f16_fp4 v197, v92, 1.0 op_sel:[1,1,0]
	v_pk_fma_f16 v187, v195, v202, v187
	v_cvt_scalef32_pk_f16_fp4 v194, v93, 1.0
	v_pk_fma_f16 v188, v196, v202, v188
	v_cvt_scalef32_pk_f16_fp4 v195, v93, 1.0 op_sel:[1,0,0]
	v_pk_fma_f16 v189, v197, v202, v189
	v_cvt_scalef32_pk_f16_fp4 v196, v93, 1.0 op_sel:[0,1,0]
	v_pk_fma_f16 v190, v194, v202, v190
	v_cvt_scalef32_pk_f16_fp4 v197, v93, 1.0 op_sel:[1,1,0]
	v_pk_fma_f16 v191, v195, v202, v191
	v_pk_fma_f16 v192, v196, v202, v192
	v_pk_fma_f16 v193, v197, v202, v193
	v_mul_u32_u24_sdwa v203, v141, s93 dst_sel:DWORD dst_unused:UNUSED_PAD src0_sel:WORD_1 src1_sel:DWORD
	v_cvt_scalef32_pk_f16_fp4 v194, v94, 1.0
	v_cvt_scalef32_pk_f16_fp4 v195, v94, 1.0 op_sel:[1,0,0]
	v_cvt_scalef32_pk_f16_fp4 v196, v94, 1.0 op_sel:[0,1,0]
	v_pk_fma_f16 v178, v194, v203, v178
	v_cvt_scalef32_pk_f16_fp4 v197, v94, 1.0 op_sel:[1,1,0]
	v_pk_fma_f16 v179, v195, v203, v179
	v_cvt_scalef32_pk_f16_fp4 v194, v95, 1.0
	v_pk_fma_f16 v180, v196, v203, v180
	v_cvt_scalef32_pk_f16_fp4 v195, v95, 1.0 op_sel:[1,0,0]
	v_pk_fma_f16 v181, v197, v203, v181
	v_cvt_scalef32_pk_f16_fp4 v196, v95, 1.0 op_sel:[0,1,0]
	v_pk_fma_f16 v182, v194, v203, v182
	v_cvt_scalef32_pk_f16_fp4 v197, v95, 1.0 op_sel:[1,1,0]
	v_pk_fma_f16 v183, v195, v203, v183
	v_cvt_scalef32_pk_f16_fp4 v194, v96, 1.0
	v_pk_fma_f16 v184, v196, v203, v184
	v_cvt_scalef32_pk_f16_fp4 v195, v96, 1.0 op_sel:[1,0,0]
	v_pk_fma_f16 v185, v197, v203, v185
	v_cvt_scalef32_pk_f16_fp4 v196, v96, 1.0 op_sel:[0,1,0]
	v_pk_fma_f16 v186, v194, v203, v186
	v_cvt_scalef32_pk_f16_fp4 v197, v96, 1.0 op_sel:[1,1,0]
	v_pk_fma_f16 v187, v195, v203, v187
	v_cvt_scalef32_pk_f16_fp4 v194, v97, 1.0
	v_pk_fma_f16 v188, v196, v203, v188
	v_cvt_scalef32_pk_f16_fp4 v195, v97, 1.0 op_sel:[1,0,0]
	v_pk_fma_f16 v189, v197, v203, v189
	v_cvt_scalef32_pk_f16_fp4 v196, v97, 1.0 op_sel:[0,1,0]
	v_pk_fma_f16 v190, v194, v203, v190
	v_cvt_scalef32_pk_f16_fp4 v197, v97, 1.0 op_sel:[1,1,0]
	v_pk_fma_f16 v191, v195, v203, v191
	v_pk_fma_f16 v192, v196, v203, v192
	v_pk_fma_f16 v193, v197, v203, v193
	v_mul_u32_u24_sdwa v202, v142, s93 dst_sel:DWORD dst_unused:UNUSED_PAD src0_sel:WORD_0 src1_sel:DWORD
	v_cvt_scalef32_pk_f16_fp4 v194, v98, 1.0
	v_cvt_scalef32_pk_f16_fp4 v195, v98, 1.0 op_sel:[1,0,0]
	v_cvt_scalef32_pk_f16_fp4 v196, v98, 1.0 op_sel:[0,1,0]
	v_pk_fma_f16 v178, v194, v202, v178
	v_cvt_scalef32_pk_f16_fp4 v197, v98, 1.0 op_sel:[1,1,0]
	v_pk_fma_f16 v179, v195, v202, v179
	v_cvt_scalef32_pk_f16_fp4 v194, v99, 1.0
	v_pk_fma_f16 v180, v196, v202, v180
	v_cvt_scalef32_pk_f16_fp4 v195, v99, 1.0 op_sel:[1,0,0]
	v_pk_fma_f16 v181, v197, v202, v181
	v_cvt_scalef32_pk_f16_fp4 v196, v99, 1.0 op_sel:[0,1,0]
	v_pk_fma_f16 v182, v194, v202, v182
	v_cvt_scalef32_pk_f16_fp4 v197, v99, 1.0 op_sel:[1,1,0]
	v_pk_fma_f16 v183, v195, v202, v183
	v_cvt_scalef32_pk_f16_fp4 v194, v100, 1.0
	v_pk_fma_f16 v184, v196, v202, v184
	v_cvt_scalef32_pk_f16_fp4 v195, v100, 1.0 op_sel:[1,0,0]
	v_pk_fma_f16 v185, v197, v202, v185
	v_cvt_scalef32_pk_f16_fp4 v196, v100, 1.0 op_sel:[0,1,0]
	v_pk_fma_f16 v186, v194, v202, v186
	v_cvt_scalef32_pk_f16_fp4 v197, v100, 1.0 op_sel:[1,1,0]
	v_pk_fma_f16 v187, v195, v202, v187
	v_cvt_scalef32_pk_f16_fp4 v194, v101, 1.0
	v_pk_fma_f16 v188, v196, v202, v188
	v_cvt_scalef32_pk_f16_fp4 v195, v101, 1.0 op_sel:[1,0,0]
	v_pk_fma_f16 v189, v197, v202, v189
	v_cvt_scalef32_pk_f16_fp4 v196, v101, 1.0 op_sel:[0,1,0]
	v_pk_fma_f16 v190, v194, v202, v190
	v_cvt_scalef32_pk_f16_fp4 v197, v101, 1.0 op_sel:[1,1,0]
	v_pk_fma_f16 v191, v195, v202, v191
	v_pk_fma_f16 v192, v196, v202, v192
	v_pk_fma_f16 v193, v197, v202, v193
	v_mul_u32_u24_sdwa v203, v142, s93 dst_sel:DWORD dst_unused:UNUSED_PAD src0_sel:WORD_1 src1_sel:DWORD
	v_cvt_scalef32_pk_f16_fp4 v194, v102, 1.0
	v_cvt_scalef32_pk_f16_fp4 v195, v102, 1.0 op_sel:[1,0,0]
	v_cvt_scalef32_pk_f16_fp4 v196, v102, 1.0 op_sel:[0,1,0]
	v_pk_fma_f16 v178, v194, v203, v178
	v_cvt_scalef32_pk_f16_fp4 v197, v102, 1.0 op_sel:[1,1,0]
	v_pk_fma_f16 v179, v195, v203, v179
	v_cvt_scalef32_pk_f16_fp4 v194, v103, 1.0
	v_pk_fma_f16 v180, v196, v203, v180
	v_cvt_scalef32_pk_f16_fp4 v195, v103, 1.0 op_sel:[1,0,0]
	v_pk_fma_f16 v181, v197, v203, v181
	v_cvt_scalef32_pk_f16_fp4 v196, v103, 1.0 op_sel:[0,1,0]
	v_pk_fma_f16 v182, v194, v203, v182
	v_cvt_scalef32_pk_f16_fp4 v197, v103, 1.0 op_sel:[1,1,0]
	v_pk_fma_f16 v183, v195, v203, v183
	v_cvt_scalef32_pk_f16_fp4 v194, v104, 1.0
	v_pk_fma_f16 v184, v196, v203, v184
	v_cvt_scalef32_pk_f16_fp4 v195, v104, 1.0 op_sel:[1,0,0]
	v_pk_fma_f16 v185, v197, v203, v185
	v_cvt_scalef32_pk_f16_fp4 v196, v104, 1.0 op_sel:[0,1,0]
	v_pk_fma_f16 v186, v194, v203, v186
	v_cvt_scalef32_pk_f16_fp4 v197, v104, 1.0 op_sel:[1,1,0]
	v_pk_fma_f16 v187, v195, v203, v187
	v_cvt_scalef32_pk_f16_fp4 v194, v105, 1.0
	v_pk_fma_f16 v188, v196, v203, v188
	v_cvt_scalef32_pk_f16_fp4 v195, v105, 1.0 op_sel:[1,0,0]
	v_pk_fma_f16 v189, v197, v203, v189
	v_cvt_scalef32_pk_f16_fp4 v196, v105, 1.0 op_sel:[0,1,0]
	v_pk_fma_f16 v190, v194, v203, v190
	v_cvt_scalef32_pk_f16_fp4 v197, v105, 1.0 op_sel:[1,1,0]
	v_pk_fma_f16 v191, v195, v203, v191
	v_pk_fma_f16 v192, v196, v203, v192
	v_pk_fma_f16 v193, v197, v203, v193
	v_mul_u32_u24_sdwa v202, v143, s93 dst_sel:DWORD dst_unused:UNUSED_PAD src0_sel:WORD_0 src1_sel:DWORD
	v_cvt_scalef32_pk_f16_fp4 v194, v106, 1.0
	v_cvt_scalef32_pk_f16_fp4 v195, v106, 1.0 op_sel:[1,0,0]
	v_cvt_scalef32_pk_f16_fp4 v196, v106, 1.0 op_sel:[0,1,0]
	v_pk_fma_f16 v178, v194, v202, v178
	v_cvt_scalef32_pk_f16_fp4 v197, v106, 1.0 op_sel:[1,1,0]
	v_pk_fma_f16 v179, v195, v202, v179
	v_cvt_scalef32_pk_f16_fp4 v194, v107, 1.0
	v_pk_fma_f16 v180, v196, v202, v180
	v_cvt_scalef32_pk_f16_fp4 v195, v107, 1.0 op_sel:[1,0,0]
	v_pk_fma_f16 v181, v197, v202, v181
	v_cvt_scalef32_pk_f16_fp4 v196, v107, 1.0 op_sel:[0,1,0]
	v_pk_fma_f16 v182, v194, v202, v182
	v_cvt_scalef32_pk_f16_fp4 v197, v107, 1.0 op_sel:[1,1,0]
	v_pk_fma_f16 v183, v195, v202, v183
	v_cvt_scalef32_pk_f16_fp4 v194, v108, 1.0
	v_pk_fma_f16 v184, v196, v202, v184
	v_cvt_scalef32_pk_f16_fp4 v195, v108, 1.0 op_sel:[1,0,0]
	v_pk_fma_f16 v185, v197, v202, v185
	v_cvt_scalef32_pk_f16_fp4 v196, v108, 1.0 op_sel:[0,1,0]
	v_pk_fma_f16 v186, v194, v202, v186
	v_cvt_scalef32_pk_f16_fp4 v197, v108, 1.0 op_sel:[1,1,0]
	v_pk_fma_f16 v187, v195, v202, v187
	v_cvt_scalef32_pk_f16_fp4 v194, v109, 1.0
	v_pk_fma_f16 v188, v196, v202, v188
	v_cvt_scalef32_pk_f16_fp4 v195, v109, 1.0 op_sel:[1,0,0]
	v_pk_fma_f16 v189, v197, v202, v189
	v_cvt_scalef32_pk_f16_fp4 v196, v109, 1.0 op_sel:[0,1,0]
	v_pk_fma_f16 v190, v194, v202, v190
	v_cvt_scalef32_pk_f16_fp4 v197, v109, 1.0 op_sel:[1,1,0]
	v_pk_fma_f16 v191, v195, v202, v191
	v_pk_fma_f16 v192, v196, v202, v192
	v_pk_fma_f16 v193, v197, v202, v193
	v_mul_u32_u24_sdwa v203, v143, s93 dst_sel:DWORD dst_unused:UNUSED_PAD src0_sel:WORD_1 src1_sel:DWORD
	v_cvt_scalef32_pk_f16_fp4 v194, v110, 1.0
	v_cvt_scalef32_pk_f16_fp4 v195, v110, 1.0 op_sel:[1,0,0]
	v_cvt_scalef32_pk_f16_fp4 v196, v110, 1.0 op_sel:[0,1,0]
	v_pk_fma_f16 v178, v194, v203, v178
	v_cvt_scalef32_pk_f16_fp4 v197, v110, 1.0 op_sel:[1,1,0]
	v_pk_fma_f16 v179, v195, v203, v179
	v_cvt_scalef32_pk_f16_fp4 v194, v111, 1.0
	v_pk_fma_f16 v180, v196, v203, v180
	v_cvt_scalef32_pk_f16_fp4 v195, v111, 1.0 op_sel:[1,0,0]
	v_pk_fma_f16 v181, v197, v203, v181
	v_cvt_scalef32_pk_f16_fp4 v196, v111, 1.0 op_sel:[0,1,0]
	v_pk_fma_f16 v182, v194, v203, v182
	v_cvt_scalef32_pk_f16_fp4 v197, v111, 1.0 op_sel:[1,1,0]
	v_pk_fma_f16 v183, v195, v203, v183
	v_cvt_scalef32_pk_f16_fp4 v194, v112, 1.0
	v_pk_fma_f16 v184, v196, v203, v184
	v_cvt_scalef32_pk_f16_fp4 v195, v112, 1.0 op_sel:[1,0,0]
	v_pk_fma_f16 v185, v197, v203, v185
	v_cvt_scalef32_pk_f16_fp4 v196, v112, 1.0 op_sel:[0,1,0]
	v_pk_fma_f16 v186, v194, v203, v186
	v_cvt_scalef32_pk_f16_fp4 v197, v112, 1.0 op_sel:[1,1,0]
	v_pk_fma_f16 v187, v195, v203, v187
	v_cvt_scalef32_pk_f16_fp4 v194, v113, 1.0
	v_pk_fma_f16 v188, v196, v203, v188
	v_cvt_scalef32_pk_f16_fp4 v195, v113, 1.0 op_sel:[1,0,0]
	v_pk_fma_f16 v189, v197, v203, v189
	v_cvt_scalef32_pk_f16_fp4 v196, v113, 1.0 op_sel:[0,1,0]
	v_pk_fma_f16 v190, v194, v203, v190
	v_cvt_scalef32_pk_f16_fp4 v197, v113, 1.0 op_sel:[1,1,0]
	v_pk_fma_f16 v191, v195, v203, v191
	v_pk_fma_f16 v192, v196, v203, v192
	v_pk_fma_f16 v193, v197, v203, v193
	v_mul_u32_u24_sdwa v202, v144, s93 dst_sel:DWORD dst_unused:UNUSED_PAD src0_sel:WORD_0 src1_sel:DWORD
	v_cvt_scalef32_pk_f16_fp4 v194, v114, 1.0
	v_cvt_scalef32_pk_f16_fp4 v195, v114, 1.0 op_sel:[1,0,0]
	v_cvt_scalef32_pk_f16_fp4 v196, v114, 1.0 op_sel:[0,1,0]
	v_pk_fma_f16 v178, v194, v202, v178
	v_cvt_scalef32_pk_f16_fp4 v197, v114, 1.0 op_sel:[1,1,0]
	v_pk_fma_f16 v179, v195, v202, v179
	v_cvt_scalef32_pk_f16_fp4 v194, v115, 1.0
	v_pk_fma_f16 v180, v196, v202, v180
	v_cvt_scalef32_pk_f16_fp4 v195, v115, 1.0 op_sel:[1,0,0]
	v_pk_fma_f16 v181, v197, v202, v181
	v_cvt_scalef32_pk_f16_fp4 v196, v115, 1.0 op_sel:[0,1,0]
	v_pk_fma_f16 v182, v194, v202, v182
	v_cvt_scalef32_pk_f16_fp4 v197, v115, 1.0 op_sel:[1,1,0]
	v_pk_fma_f16 v183, v195, v202, v183
	v_cvt_scalef32_pk_f16_fp4 v194, v116, 1.0
	v_pk_fma_f16 v184, v196, v202, v184
	v_cvt_scalef32_pk_f16_fp4 v195, v116, 1.0 op_sel:[1,0,0]
	v_pk_fma_f16 v185, v197, v202, v185
	v_cvt_scalef32_pk_f16_fp4 v196, v116, 1.0 op_sel:[0,1,0]
	v_pk_fma_f16 v186, v194, v202, v186
	v_cvt_scalef32_pk_f16_fp4 v197, v116, 1.0 op_sel:[1,1,0]
	v_pk_fma_f16 v187, v195, v202, v187
	v_cvt_scalef32_pk_f16_fp4 v194, v117, 1.0
	v_pk_fma_f16 v188, v196, v202, v188
	v_cvt_scalef32_pk_f16_fp4 v195, v117, 1.0 op_sel:[1,0,0]
	v_pk_fma_f16 v189, v197, v202, v189
	v_cvt_scalef32_pk_f16_fp4 v196, v117, 1.0 op_sel:[0,1,0]
	v_pk_fma_f16 v190, v194, v202, v190
	v_cvt_scalef32_pk_f16_fp4 v197, v117, 1.0 op_sel:[1,1,0]
	v_pk_fma_f16 v191, v195, v202, v191
	v_pk_fma_f16 v192, v196, v202, v192
	v_pk_fma_f16 v193, v197, v202, v193
	v_mul_u32_u24_sdwa v203, v144, s93 dst_sel:DWORD dst_unused:UNUSED_PAD src0_sel:WORD_1 src1_sel:DWORD
	v_cvt_scalef32_pk_f16_fp4 v194, v118, 1.0
	v_cvt_scalef32_pk_f16_fp4 v195, v118, 1.0 op_sel:[1,0,0]
	v_cvt_scalef32_pk_f16_fp4 v196, v118, 1.0 op_sel:[0,1,0]
	v_pk_fma_f16 v178, v194, v203, v178
	v_cvt_scalef32_pk_f16_fp4 v197, v118, 1.0 op_sel:[1,1,0]
	v_pk_fma_f16 v179, v195, v203, v179
	v_cvt_scalef32_pk_f16_fp4 v194, v119, 1.0
	v_pk_fma_f16 v180, v196, v203, v180
	v_cvt_scalef32_pk_f16_fp4 v195, v119, 1.0 op_sel:[1,0,0]
	v_pk_fma_f16 v181, v197, v203, v181
	v_cvt_scalef32_pk_f16_fp4 v196, v119, 1.0 op_sel:[0,1,0]
	v_pk_fma_f16 v182, v194, v203, v182
	v_cvt_scalef32_pk_f16_fp4 v197, v119, 1.0 op_sel:[1,1,0]
	v_pk_fma_f16 v183, v195, v203, v183
	v_cvt_scalef32_pk_f16_fp4 v194, v120, 1.0
	v_pk_fma_f16 v184, v196, v203, v184
	v_cvt_scalef32_pk_f16_fp4 v195, v120, 1.0 op_sel:[1,0,0]
	v_pk_fma_f16 v185, v197, v203, v185
	v_cvt_scalef32_pk_f16_fp4 v196, v120, 1.0 op_sel:[0,1,0]
	v_pk_fma_f16 v186, v194, v203, v186
	v_cvt_scalef32_pk_f16_fp4 v197, v120, 1.0 op_sel:[1,1,0]
	v_pk_fma_f16 v187, v195, v203, v187
	v_cvt_scalef32_pk_f16_fp4 v194, v121, 1.0
	v_pk_fma_f16 v188, v196, v203, v188
	v_cvt_scalef32_pk_f16_fp4 v195, v121, 1.0 op_sel:[1,0,0]
	v_pk_fma_f16 v189, v197, v203, v189
	v_cvt_scalef32_pk_f16_fp4 v196, v121, 1.0 op_sel:[0,1,0]
	v_pk_fma_f16 v190, v194, v203, v190
	v_cvt_scalef32_pk_f16_fp4 v197, v121, 1.0 op_sel:[1,1,0]
	v_pk_fma_f16 v191, v195, v203, v191
	v_pk_fma_f16 v192, v196, v203, v192
	v_pk_fma_f16 v193, v197, v203, v193
	v_mul_u32_u24_sdwa v202, v145, s93 dst_sel:DWORD dst_unused:UNUSED_PAD src0_sel:WORD_0 src1_sel:DWORD
	v_cvt_scalef32_pk_f16_fp4 v194, v122, 1.0
	v_cvt_scalef32_pk_f16_fp4 v195, v122, 1.0 op_sel:[1,0,0]
	v_cvt_scalef32_pk_f16_fp4 v196, v122, 1.0 op_sel:[0,1,0]
	v_pk_fma_f16 v178, v194, v202, v178
	v_cvt_scalef32_pk_f16_fp4 v197, v122, 1.0 op_sel:[1,1,0]
	v_pk_fma_f16 v179, v195, v202, v179
	v_cvt_scalef32_pk_f16_fp4 v194, v123, 1.0
	v_pk_fma_f16 v180, v196, v202, v180
	v_cvt_scalef32_pk_f16_fp4 v195, v123, 1.0 op_sel:[1,0,0]
	v_pk_fma_f16 v181, v197, v202, v181
	v_cvt_scalef32_pk_f16_fp4 v196, v123, 1.0 op_sel:[0,1,0]
	v_pk_fma_f16 v182, v194, v202, v182
	v_cvt_scalef32_pk_f16_fp4 v197, v123, 1.0 op_sel:[1,1,0]
	v_pk_fma_f16 v183, v195, v202, v183
	v_cvt_scalef32_pk_f16_fp4 v194, v124, 1.0
	v_pk_fma_f16 v184, v196, v202, v184
	v_cvt_scalef32_pk_f16_fp4 v195, v124, 1.0 op_sel:[1,0,0]
	v_pk_fma_f16 v185, v197, v202, v185
	v_cvt_scalef32_pk_f16_fp4 v196, v124, 1.0 op_sel:[0,1,0]
	v_pk_fma_f16 v186, v194, v202, v186
	v_cvt_scalef32_pk_f16_fp4 v197, v124, 1.0 op_sel:[1,1,0]
	v_pk_fma_f16 v187, v195, v202, v187
	v_cvt_scalef32_pk_f16_fp4 v194, v125, 1.0
	v_pk_fma_f16 v188, v196, v202, v188
	v_cvt_scalef32_pk_f16_fp4 v195, v125, 1.0 op_sel:[1,0,0]
	v_pk_fma_f16 v189, v197, v202, v189
	v_cvt_scalef32_pk_f16_fp4 v196, v125, 1.0 op_sel:[0,1,0]
	v_pk_fma_f16 v190, v194, v202, v190
	v_cvt_scalef32_pk_f16_fp4 v197, v125, 1.0 op_sel:[1,1,0]
	v_pk_fma_f16 v191, v195, v202, v191
	v_pk_fma_f16 v192, v196, v202, v192
	v_pk_fma_f16 v193, v197, v202, v193
	v_mul_u32_u24_sdwa v203, v145, s93 dst_sel:DWORD dst_unused:UNUSED_PAD src0_sel:WORD_1 src1_sel:DWORD
	v_cvt_scalef32_pk_f16_fp4 v194, v126, 1.0
	v_cvt_scalef32_pk_f16_fp4 v195, v126, 1.0 op_sel:[1,0,0]
	v_cvt_scalef32_pk_f16_fp4 v196, v126, 1.0 op_sel:[0,1,0]
	v_pk_fma_f16 v178, v194, v203, v178
	v_cvt_scalef32_pk_f16_fp4 v197, v126, 1.0 op_sel:[1,1,0]
	v_pk_fma_f16 v179, v195, v203, v179
	v_cvt_scalef32_pk_f16_fp4 v194, v127, 1.0
	v_pk_fma_f16 v180, v196, v203, v180
	v_cvt_scalef32_pk_f16_fp4 v195, v127, 1.0 op_sel:[1,0,0]
	v_pk_fma_f16 v181, v197, v203, v181
	v_cvt_scalef32_pk_f16_fp4 v196, v127, 1.0 op_sel:[0,1,0]
	v_pk_fma_f16 v182, v194, v203, v182
	v_cvt_scalef32_pk_f16_fp4 v197, v127, 1.0 op_sel:[1,1,0]
	v_pk_fma_f16 v183, v195, v203, v183
	v_cvt_scalef32_pk_f16_fp4 v194, v128, 1.0
	v_pk_fma_f16 v184, v196, v203, v184
	v_cvt_scalef32_pk_f16_fp4 v195, v128, 1.0 op_sel:[1,0,0]
	v_pk_fma_f16 v185, v197, v203, v185
	v_cvt_scalef32_pk_f16_fp4 v196, v128, 1.0 op_sel:[0,1,0]
	v_pk_fma_f16 v186, v194, v203, v186
	v_cvt_scalef32_pk_f16_fp4 v197, v128, 1.0 op_sel:[1,1,0]
	v_pk_fma_f16 v187, v195, v203, v187
	v_cvt_scalef32_pk_f16_fp4 v194, v129, 1.0
	v_pk_fma_f16 v188, v196, v203, v188
	v_cvt_scalef32_pk_f16_fp4 v195, v129, 1.0 op_sel:[1,0,0]
	v_pk_fma_f16 v189, v197, v203, v189
	v_cvt_scalef32_pk_f16_fp4 v196, v129, 1.0 op_sel:[0,1,0]
	v_pk_fma_f16 v190, v194, v203, v190
	v_cvt_scalef32_pk_f16_fp4 v197, v129, 1.0 op_sel:[1,1,0]
	v_pk_fma_f16 v191, v195, v203, v191
	v_pk_fma_f16 v192, v196, v203, v192
	v_pk_fma_f16 v193, v197, v203, v193
	s_nop 1
	v_permlane32_swap_b32_e32 v178, v186
	v_permlane32_swap_b32_e32 v179, v187
	v_permlane32_swap_b32_e32 v180, v188
	v_permlane32_swap_b32_e32 v181, v189
	v_permlane32_swap_b32_e32 v182, v190
	v_permlane32_swap_b32_e32 v183, v191
	v_permlane32_swap_b32_e32 v184, v192
	v_permlane32_swap_b32_e32 v185, v193
	v_pk_add_f16 v66, v178, v186
	v_pk_add_f16 v67, v179, v187
	v_pk_add_f16 v68, v180, v188
	v_pk_add_f16 v69, v181, v189
	v_pk_add_f16 v70, v182, v190
	v_pk_add_f16 v71, v183, v191
	v_pk_add_f16 v72, v184, v192
	v_pk_add_f16 v73, v185, v193
	v_cvt_f32_f16_e32 v74, v66
	v_cvt_f32_f16_sdwa v75, v66 dst_sel:DWORD dst_unused:UNUSED_PAD src0_sel:WORD_1
	v_cvt_f32_f16_e32 v76, v67
	v_cvt_f32_f16_sdwa v77, v67 dst_sel:DWORD dst_unused:UNUSED_PAD src0_sel:WORD_1
	v_cvt_f32_f16_e32 v78, v68
	v_cvt_f32_f16_sdwa v79, v68 dst_sel:DWORD dst_unused:UNUSED_PAD src0_sel:WORD_1
	v_cvt_f32_f16_e32 v80, v69
	v_cvt_f32_f16_sdwa v81, v69 dst_sel:DWORD dst_unused:UNUSED_PAD src0_sel:WORD_1
	v_cvt_f32_f16_e32 v82, v70
	v_cvt_f32_f16_sdwa v83, v70 dst_sel:DWORD dst_unused:UNUSED_PAD src0_sel:WORD_1
	v_cvt_f32_f16_e32 v84, v71
	v_cvt_f32_f16_sdwa v85, v71 dst_sel:DWORD dst_unused:UNUSED_PAD src0_sel:WORD_1
	v_cvt_f32_f16_e32 v86, v72
	v_cvt_f32_f16_sdwa v87, v72 dst_sel:DWORD dst_unused:UNUSED_PAD src0_sel:WORD_1
	v_cvt_f32_f16_e32 v88, v73
	v_cvt_f32_f16_sdwa v89, v73 dst_sel:DWORD dst_unused:UNUSED_PAD src0_sel:WORD_1
	s_nop 1
	v_permlane16_swap_b32_e32 v74, v82
	v_permlane16_swap_b32_e32 v75, v83
	v_permlane16_swap_b32_e32 v76, v84
	v_permlane16_swap_b32_e32 v77, v85
	v_permlane16_swap_b32_e32 v78, v86
	v_permlane16_swap_b32_e32 v79, v87
	v_permlane16_swap_b32_e32 v80, v88
	v_permlane16_swap_b32_e32 v81, v89
	v_add_f32_e32 v90, v74, v82
	v_add_f32_e32 v91, v75, v83
	v_add_f32_e32 v92, v76, v84
	v_add_f32_e32 v93, v77, v85
	v_add_f32_e32 v94, v78, v86
	v_add_f32_e32 v95, v79, v87
	v_add_f32_e32 v96, v80, v88
	v_add_f32_e32 v97, v81, v89
	s_nop 1
	v_add_f32_dpp v98, v90, v90 row_ror:8 row_mask:0xf bank_mask:0xf bound_ctrl:1
	v_add_f32_dpp v99, v94, v94 row_ror:8 row_mask:0xf bank_mask:0xf bound_ctrl:1
	v_add_f32_dpp v100, v91, v91 row_ror:8 row_mask:0xf bank_mask:0xf bound_ctrl:1
	v_add_f32_dpp v101, v95, v95 row_ror:8 row_mask:0xf bank_mask:0xf bound_ctrl:1
	v_add_f32_dpp v102, v92, v92 row_ror:8 row_mask:0xf bank_mask:0xf bound_ctrl:1
	v_add_f32_dpp v103, v96, v96 row_ror:8 row_mask:0xf bank_mask:0xf bound_ctrl:1
	v_add_f32_dpp v104, v93, v93 row_ror:8 row_mask:0xf bank_mask:0xf bound_ctrl:1
	v_add_f32_dpp v105, v97, v97 row_ror:8 row_mask:0xf bank_mask:0xf bound_ctrl:1
	v_cndmask_b32_e64 v106, v99, v98, s[38:39]
	v_cndmask_b32_e64 v107, v101, v100, s[38:39]
	v_cndmask_b32_e64 v108, v103, v102, s[38:39]
	v_cndmask_b32_e64 v109, v105, v104, s[38:39]
	v_fma_f32 v110, v158, v106, v154
	v_fma_f32 v111, v159, v107, v155
	v_fma_f32 v112, v160, v108, v156
	v_fma_f32 v113, v161, v109, v157
	global_store_dwordx4 v[240:241], v[110:113], off
	v_add_u32_e32 v226, 2, v226
	s_add_i32 s33, s33, 2
	s_cmp_lt_u32 s33, 8
	s_cbranch_scc1 .Le2_loop
	s_cmp_lt_i32 s35, 0
	s_cbranch_scc1 .Le2_chain_end
	s_mov_b32 s33, 0
	s_branch .Le2_loop
